# grid barrier: flattened release plus leader invalidate issued after the arrival result is read and never waited on before the release
# speedup vs baseline: 1.0025x; 1.0021x over previous
.LBB0_188:
	s_or_b64 exec, exec, s[8:9]
	v_cvt_f32_u32_e32 v3, v0
	s_waitcnt vmcnt(0)
	v_readfirstlane_b32 s4, v2
	buffer_inv sc1
	s_add_u32 s8, s46, 0x7500
	s_addc_u32 s9, s47, 0
	v_rcp_iflag_f32_e32 v3, v3
	v_add_u32_e32 v1, s4, v1
	v_add_u32_e32 v4, 1, v1
	s_mov_b64 s[10:11], -1
	v_mul_f32_e32 v2, 0x4f7ffffe, v3
	v_cvt_u32_f32_e32 v2, v2
	v_sub_u32_e32 v3, 0, v0
	v_mul_lo_u32 v3, v3, v2
	v_mul_hi_u32 v3, v2, v3
	v_add_u32_e32 v2, v2, v3
	v_mul_hi_u32 v2, v1, v2
	v_mul_lo_u32 v3, v2, v0
	v_sub_u32_e32 v1, v1, v3
	v_add_u32_e32 v5, 1, v2
	v_cmp_ge_u32_e32 vcc, v1, v0
	v_sub_u32_e32 v3, v1, v0
	s_nop 0
	v_cndmask_b32_e32 v2, v2, v5, vcc
	v_cndmask_b32_e32 v1, v1, v3, vcc
	v_add_u32_e32 v3, 1, v2
	v_cmp_ge_u32_e32 vcc, v1, v0
	s_nop 1
	v_cndmask_b32_e32 v2, v2, v3, vcc
	v_mul_lo_u32 v1, v0, v2
	v_add_u32_e32 v0, v1, v0
	v_cmp_ne_u32_e32 vcc, v4, v0
	s_cbranch_vccnz .Lxr_0
	v_readlane_b32 s98, v254, 9
	v_readlane_b32 s99, v254, 10
	v_mov_b32_e32 v100, 0x2400
	v_mov_b32_e32 v101, 1
	s_nop 4
	global_atomic_add v100, v101, s[98:99]
	global_atomic_add v100, v101, s[98:99] offset:256
	global_atomic_add v100, v101, s[98:99] offset:512
	global_atomic_add v100, v101, s[98:99] offset:768
	global_atomic_add v100, v101, s[98:99] offset:1024
	global_atomic_add v100, v101, s[98:99] offset:1280
	global_atomic_add v100, v101, s[98:99] offset:1536
	global_atomic_add v100, v101, s[98:99] offset:1792
	global_atomic_add v100, v101, s[98:99] offset:2048
	global_atomic_add v100, v101, s[98:99] offset:2304
	global_atomic_add v100, v101, s[98:99] offset:2560
	global_atomic_add v100, v101, s[98:99] offset:2816
	global_atomic_add v100, v101, s[98:99] offset:3072
	global_atomic_add v100, v101, s[98:99] offset:3328
	global_atomic_add v100, v101, s[98:99] offset:3584
	global_atomic_add v100, v101, s[98:99] offset:3840

.LBB0_306:
	s_or_b64 exec, exec, s[6:7]
	s_waitcnt vmcnt(0)
	v_readfirstlane_b32 s4, v3
	buffer_inv sc1
	v_sub_u32_e32 v4, 0, v2
	s_mov_b64 s[14:15], -1
	v_add_u32_e32 v3, s4, v0
	v_cvt_f32_u32_e32 v0, v2
	v_readlane_b32 s4, v254, 46
	v_readlane_b32 s5, v254, 47
	s_add_u32 s4, s4, 0x3500
	v_rcp_iflag_f32_e32 v0, v0
	s_addc_u32 s5, s5, 0
	v_mul_f32_e32 v0, 0x4f7ffffe, v0
	v_cvt_u32_f32_e32 v0, v0
	v_mul_lo_u32 v4, v4, v0
	v_mul_hi_u32 v4, v0, v4
	v_add_u32_e32 v0, v0, v4
	v_mul_hi_u32 v0, v3, v0
	v_mul_lo_u32 v4, v0, v2
	v_sub_u32_e32 v4, v3, v4
	v_cmp_ge_u32_e32 vcc, v4, v2
	v_add_u32_e32 v5, 1, v0
	v_add_u32_e32 v3, 1, v3
	v_cndmask_b32_e32 v0, v0, v5, vcc
	v_sub_u32_e32 v5, v4, v2
	v_cndmask_b32_e32 v4, v4, v5, vcc
	v_cmp_ge_u32_e32 vcc, v4, v2
	v_add_u32_e32 v4, 1, v0
	s_nop 0
	v_cndmask_b32_e32 v0, v0, v4, vcc
	v_mul_lo_u32 v4, v2, v0
	v_add_u32_e32 v2, v4, v2
	v_cmp_ne_u32_e32 vcc, v3, v2
	s_cbranch_vccnz .Lxr_1
	v_readlane_b32 s98, v254, 9
	v_readlane_b32 s99, v254, 10
	v_mov_b32_e32 v100, 0x2400
	v_mov_b32_e32 v101, 1
	s_nop 4
	global_atomic_add v100, v101, s[98:99]
	global_atomic_add v100, v101, s[98:99] offset:256
	global_atomic_add v100, v101, s[98:99] offset:512
	global_atomic_add v100, v101, s[98:99] offset:768
	global_atomic_add v100, v101, s[98:99] offset:1024
	global_atomic_add v100, v101, s[98:99] offset:1280
	global_atomic_add v100, v101, s[98:99] offset:1536
	global_atomic_add v100, v101, s[98:99] offset:1792
	global_atomic_add v100, v101, s[98:99] offset:2048
	global_atomic_add v100, v101, s[98:99] offset:2304
	global_atomic_add v100, v101, s[98:99] offset:2560
	global_atomic_add v100, v101, s[98:99] offset:2816
	global_atomic_add v100, v101, s[98:99] offset:3072
	global_atomic_add v100, v101, s[98:99] offset:3328
	global_atomic_add v100, v101, s[98:99] offset:3584
	global_atomic_add v100, v101, s[98:99] offset:3840

.LBB0_645:
	s_or_b64 exec, exec, s[6:7]
	s_waitcnt vmcnt(0)
	v_readfirstlane_b32 s2, v3
	buffer_inv sc1
	v_sub_u32_e32 v4, 0, v2
	s_mov_b64 s[14:15], -1
	v_add_u32_e32 v3, s2, v0
	v_cvt_f32_u32_e32 v0, v2
	v_readlane_b32 s2, v254, 46
	v_readlane_b32 s3, v254, 47
	s_add_u32 s2, s2, 0x3500
	v_rcp_iflag_f32_e32 v0, v0
	s_addc_u32 s3, s3, 0
	v_mul_f32_e32 v0, 0x4f7ffffe, v0
	v_cvt_u32_f32_e32 v0, v0
	v_mul_lo_u32 v4, v4, v0
	v_mul_hi_u32 v4, v0, v4
	v_add_u32_e32 v0, v0, v4
	v_mul_hi_u32 v0, v3, v0
	v_mul_lo_u32 v4, v0, v2
	v_sub_u32_e32 v4, v3, v4
	v_cmp_ge_u32_e32 vcc, v4, v2
	v_add_u32_e32 v5, 1, v0
	v_add_u32_e32 v3, 1, v3
	v_cndmask_b32_e32 v0, v0, v5, vcc
	v_sub_u32_e32 v5, v4, v2
	v_cndmask_b32_e32 v4, v4, v5, vcc
	v_cmp_ge_u32_e32 vcc, v4, v2
	v_add_u32_e32 v4, 1, v0
	s_nop 0
	v_cndmask_b32_e32 v0, v0, v4, vcc
	v_mul_lo_u32 v4, v2, v0
	v_add_u32_e32 v2, v4, v2
	v_cmp_ne_u32_e32 vcc, v3, v2
	s_cbranch_vccnz .Lxr_2
	v_readlane_b32 s98, v254, 9
	v_readlane_b32 s99, v254, 10
	v_mov_b32_e32 v100, 0x2400
	v_mov_b32_e32 v101, 1
	s_nop 4
	global_atomic_add v100, v101, s[98:99]
	global_atomic_add v100, v101, s[98:99] offset:256
	global_atomic_add v100, v101, s[98:99] offset:512
	global_atomic_add v100, v101, s[98:99] offset:768
	global_atomic_add v100, v101, s[98:99] offset:1024
	global_atomic_add v100, v101, s[98:99] offset:1280
	global_atomic_add v100, v101, s[98:99] offset:1536
	global_atomic_add v100, v101, s[98:99] offset:1792
	global_atomic_add v100, v101, s[98:99] offset:2048
	global_atomic_add v100, v101, s[98:99] offset:2304
	global_atomic_add v100, v101, s[98:99] offset:2560
	global_atomic_add v100, v101, s[98:99] offset:2816
	global_atomic_add v100, v101, s[98:99] offset:3072
	global_atomic_add v100, v101, s[98:99] offset:3328
	global_atomic_add v100, v101, s[98:99] offset:3584
	global_atomic_add v100, v101, s[98:99] offset:3840

.LBB0_811:
	s_or_b64 exec, exec, s[10:11]
	s_waitcnt vmcnt(0)
	v_readfirstlane_b32 s6, v3
	buffer_inv sc1
	v_sub_u32_e32 v4, 0, v2
	s_mov_b64 s[12:13], -1
	v_add_u32_e32 v3, s6, v0
	v_cvt_f32_u32_e32 v0, v2
	v_readlane_b32 s6, v254, 46
	v_readlane_b32 s7, v254, 47
	s_add_u32 s6, s6, 0x3500
	v_rcp_iflag_f32_e32 v0, v0
	s_addc_u32 s7, s7, 0
	v_mul_f32_e32 v0, 0x4f7ffffe, v0
	v_cvt_u32_f32_e32 v0, v0
	v_mul_lo_u32 v4, v4, v0
	v_mul_hi_u32 v4, v0, v4
	v_add_u32_e32 v0, v0, v4
	v_mul_hi_u32 v0, v3, v0
	v_mul_lo_u32 v4, v0, v2
	v_sub_u32_e32 v4, v3, v4
	v_cmp_ge_u32_e32 vcc, v4, v2
	v_add_u32_e32 v5, 1, v0
	v_add_u32_e32 v3, 1, v3
	v_cndmask_b32_e32 v0, v0, v5, vcc
	v_sub_u32_e32 v5, v4, v2
	v_cndmask_b32_e32 v4, v4, v5, vcc
	v_cmp_ge_u32_e32 vcc, v4, v2
	v_add_u32_e32 v4, 1, v0
	s_nop 0
	v_cndmask_b32_e32 v0, v0, v4, vcc
	v_mul_lo_u32 v4, v2, v0
	v_add_u32_e32 v2, v4, v2
	v_cmp_ne_u32_e32 vcc, v3, v2
	s_cbranch_vccnz .Lxr_3
	v_readlane_b32 s98, v254, 9
	v_readlane_b32 s99, v254, 10
	v_mov_b32_e32 v100, 0x2400
	v_mov_b32_e32 v101, 1
	s_nop 4
	global_atomic_add v100, v101, s[98:99]
	global_atomic_add v100, v101, s[98:99] offset:256
	global_atomic_add v100, v101, s[98:99] offset:512
	global_atomic_add v100, v101, s[98:99] offset:768
	global_atomic_add v100, v101, s[98:99] offset:1024
	global_atomic_add v100, v101, s[98:99] offset:1280
	global_atomic_add v100, v101, s[98:99] offset:1536
	global_atomic_add v100, v101, s[98:99] offset:1792
	global_atomic_add v100, v101, s[98:99] offset:2048
	global_atomic_add v100, v101, s[98:99] offset:2304
	global_atomic_add v100, v101, s[98:99] offset:2560
	global_atomic_add v100, v101, s[98:99] offset:2816
	global_atomic_add v100, v101, s[98:99] offset:3072
	global_atomic_add v100, v101, s[98:99] offset:3328
	global_atomic_add v100, v101, s[98:99] offset:3584
	global_atomic_add v100, v101, s[98:99] offset:3840

.LBB0_914:
	s_or_b64 exec, exec, s[4:5]
	s_waitcnt vmcnt(0)
	v_readfirstlane_b32 s2, v3
	buffer_inv sc1
	v_sub_u32_e32 v4, 0, v2
	s_mov_b64 s[6:7], -1
	v_add_u32_e32 v3, s2, v0
	v_cvt_f32_u32_e32 v0, v2
	v_readlane_b32 s2, v254, 46
	v_readlane_b32 s3, v254, 47
	s_add_u32 s2, s2, 0x3500
	v_rcp_iflag_f32_e32 v0, v0
	s_addc_u32 s3, s3, 0
	v_mul_f32_e32 v0, 0x4f7ffffe, v0
	v_cvt_u32_f32_e32 v0, v0
	v_mul_lo_u32 v4, v4, v0
	v_mul_hi_u32 v4, v0, v4
	v_add_u32_e32 v0, v0, v4
	v_mul_hi_u32 v0, v3, v0
	v_mul_lo_u32 v4, v0, v2
	v_sub_u32_e32 v4, v3, v4
	v_cmp_ge_u32_e32 vcc, v4, v2
	v_add_u32_e32 v5, 1, v0
	v_add_u32_e32 v3, 1, v3
	v_cndmask_b32_e32 v0, v0, v5, vcc
	v_sub_u32_e32 v5, v4, v2
	v_cndmask_b32_e32 v4, v4, v5, vcc
	v_cmp_ge_u32_e32 vcc, v4, v2
	v_add_u32_e32 v4, 1, v0
	s_nop 0
	v_cndmask_b32_e32 v0, v0, v4, vcc
	v_mul_lo_u32 v4, v2, v0
	v_add_u32_e32 v2, v4, v2
	v_cmp_ne_u32_e32 vcc, v3, v2
	s_cbranch_vccnz .Lxr_4
	v_readlane_b32 s98, v254, 9
	v_readlane_b32 s99, v254, 10
	v_mov_b32_e32 v100, 0x2400
	v_mov_b32_e32 v101, 1
	s_nop 4
	global_atomic_add v100, v101, s[98:99]
	global_atomic_add v100, v101, s[98:99] offset:256
	global_atomic_add v100, v101, s[98:99] offset:512
	global_atomic_add v100, v101, s[98:99] offset:768
	global_atomic_add v100, v101, s[98:99] offset:1024
	global_atomic_add v100, v101, s[98:99] offset:1280
	global_atomic_add v100, v101, s[98:99] offset:1536
	global_atomic_add v100, v101, s[98:99] offset:1792
	global_atomic_add v100, v101, s[98:99] offset:2048
	global_atomic_add v100, v101, s[98:99] offset:2304
	global_atomic_add v100, v101, s[98:99] offset:2560
	global_atomic_add v100, v101, s[98:99] offset:2816
	global_atomic_add v100, v101, s[98:99] offset:3072
	global_atomic_add v100, v101, s[98:99] offset:3328
	global_atomic_add v100, v101, s[98:99] offset:3584
	global_atomic_add v100, v101, s[98:99] offset:3840

.LBB0_1114:
	s_or_b64 exec, exec, s[6:7]
	s_waitcnt vmcnt(0)
	v_readfirstlane_b32 s4, v3
	buffer_inv sc1
	v_sub_u32_e32 v4, 0, v2
	s_mov_b64 s[8:9], -1
	v_add_u32_e32 v3, s4, v0
	v_cvt_f32_u32_e32 v0, v2
	v_readlane_b32 s4, v254, 46
	v_readlane_b32 s5, v254, 47
	s_add_u32 s4, s4, 0x3500
	v_rcp_iflag_f32_e32 v0, v0
	s_addc_u32 s5, s5, 0
	v_mul_f32_e32 v0, 0x4f7ffffe, v0
	v_cvt_u32_f32_e32 v0, v0
	v_mul_lo_u32 v4, v4, v0
	v_mul_hi_u32 v4, v0, v4
	v_add_u32_e32 v0, v0, v4
	v_mul_hi_u32 v0, v3, v0
	v_mul_lo_u32 v4, v0, v2
	v_sub_u32_e32 v4, v3, v4
	v_cmp_ge_u32_e32 vcc, v4, v2
	v_add_u32_e32 v5, 1, v0
	v_add_u32_e32 v3, 1, v3
	v_cndmask_b32_e32 v0, v0, v5, vcc
	v_sub_u32_e32 v5, v4, v2
	v_cndmask_b32_e32 v4, v4, v5, vcc
	v_cmp_ge_u32_e32 vcc, v4, v2
	v_add_u32_e32 v4, 1, v0
	s_nop 0
	v_cndmask_b32_e32 v0, v0, v4, vcc
	v_mul_lo_u32 v4, v2, v0
	v_add_u32_e32 v2, v4, v2
	v_cmp_ne_u32_e32 vcc, v3, v2
	s_cbranch_vccnz .Lxr_5
	v_readlane_b32 s98, v254, 9
	v_readlane_b32 s99, v254, 10
	v_mov_b32_e32 v100, 0x2400
	v_mov_b32_e32 v101, 1
	s_nop 4
	global_atomic_add v100, v101, s[98:99]
	global_atomic_add v100, v101, s[98:99] offset:256
	global_atomic_add v100, v101, s[98:99] offset:512
	global_atomic_add v100, v101, s[98:99] offset:768
	global_atomic_add v100, v101, s[98:99] offset:1024
	global_atomic_add v100, v101, s[98:99] offset:1280
	global_atomic_add v100, v101, s[98:99] offset:1536
	global_atomic_add v100, v101, s[98:99] offset:1792
	global_atomic_add v100, v101, s[98:99] offset:2048
	global_atomic_add v100, v101, s[98:99] offset:2304
	global_atomic_add v100, v101, s[98:99] offset:2560
	global_atomic_add v100, v101, s[98:99] offset:2816
	global_atomic_add v100, v101, s[98:99] offset:3072
	global_atomic_add v100, v101, s[98:99] offset:3328
	global_atomic_add v100, v101, s[98:99] offset:3584
	global_atomic_add v100, v101, s[98:99] offset:3840
